# speedup vs baseline: 1.0239x; 1.0239x over previous
.LBB0_120:
	s_cmpk_gt_u32 s33, 0x7f
	s_waitcnt lgkmcnt(0)
	s_cbranch_scc1 .Lmlp_others
	v_mbcnt_lo_u32_b32 v92, -1, 0
	v_mbcnt_hi_u32_b32 v92, -1, v92
	v_mov_b32_e32 v1, 0x15300
	v_ashrrev_i32_e32 v0, 5, v92
	s_waitcnt vmcnt(0)
	v_and_or_b32 v37, v92, 31, s31
	v_lshlrev_b32_e32 v38, 4, v0
	v_lshl_add_u32 v1, v37, 2, v1
	v_add_u32_e32 v93, 0x14c00, v38
	ds_read_b32 v36, v1
	ds_read_b128 v[0:3], v93
	ds_read_b128 v[4:7], v93 offset:32
	ds_read_b128 v[8:11], v93 offset:64
	v_add_u32_e32 v39, v93, v38
	ds_read_b128 v[24:27], v39 offset:1280
	ds_read_b128 v[28:31], v39 offset:1024
	ds_read_b128 v[12:15], v93 offset:96
	ds_read_b128 v[16:19], v93 offset:128
	ds_read_b128 v[20:23], v39 offset:1040
	ds_read_b128 v[32:35], v39 offset:1232
	ds_read_b128 v[80:83], v93 offset:992
	s_waitcnt lgkmcnt(5)
	v_fma_f32 v24, v36, v28, v24
	v_max_f32_e32 v44, 0, v24
	v_fma_f32 v24, v36, v29, v25
	ds_read_b128 v[40:43], v39 offset:1296
	v_max_f32_e32 v45, 0, v24
	v_fma_f32 v24, v36, v30, v26
	v_fmac_f32_e32 v27, v36, v31
	v_max_f32_e32 v46, 0, v24
	v_max_f32_e32 v47, 0, v27
	ds_read_b128 v[24:27], v39 offset:1088
	ds_read_b128 v[28:31], v39 offset:1344
	s_waitcnt lgkmcnt(2)
	v_fma_f32 v20, v36, v20, v40
	v_fma_f32 v21, v36, v21, v41
	v_max_f32_e32 v20, 0, v20
	v_max_f32_e32 v21, 0, v21
	v_fma_f32 v22, v36, v22, v42
	v_cvt_pk_f16_f32 v42, v20, v21
	s_waitcnt lgkmcnt(0)
	v_fma_f32 v20, v36, v24, v28
	v_fmac_f32_e32 v43, v36, v23
	v_max_f32_e32 v48, 0, v20
	v_fma_f32 v20, v36, v25, v29
	v_max_f32_e32 v22, 0, v22
	v_max_f32_e32 v23, 0, v43
	v_max_f32_e32 v49, 0, v20
	v_fma_f32 v20, v36, v26, v30
	v_cvt_pk_f16_f32 v43, v22, v23
	v_cvt_pk_f16_f32 v41, v46, v47
	v_cvt_pk_f16_f32 v40, v44, v45
	v_max_f32_e32 v50, 0, v20
	ds_read_b128 v[20:23], v39 offset:1104
	ds_read_b128 v[44:47], v39 offset:1360
	v_fmac_f32_e32 v31, v36, v27
	v_max_f32_e32 v51, 0, v31
	ds_read_b128 v[24:27], v39 offset:1152
	ds_read_b128 v[28:31], v39 offset:1408
	v_lshlrev_b32_e32 v94, 4, v92
	s_waitcnt lgkmcnt(2)
	v_fma_f32 v20, v36, v20, v44
	v_fma_f32 v21, v36, v21, v45
	v_max_f32_e32 v20, 0, v20
	v_max_f32_e32 v21, 0, v21
	v_fma_f32 v22, v36, v22, v46
	v_cvt_pk_f16_f32 v46, v20, v21
	s_waitcnt lgkmcnt(0)
	v_fma_f32 v20, v36, v24, v28
	v_fmac_f32_e32 v47, v36, v23
	v_max_f32_e32 v52, 0, v20
	v_fma_f32 v20, v36, v25, v29
	v_max_f32_e32 v22, 0, v22
	v_max_f32_e32 v23, 0, v47
	v_max_f32_e32 v53, 0, v20
	v_fma_f32 v20, v36, v26, v30
	v_cvt_pk_f16_f32 v47, v22, v23
	v_cvt_pk_f16_f32 v45, v50, v51
	v_cvt_pk_f16_f32 v44, v48, v49
	v_max_f32_e32 v54, 0, v20
	ds_read_b128 v[20:23], v39 offset:1168
	ds_read_b128 v[48:51], v39 offset:1424
	v_fmac_f32_e32 v31, v36, v27
	v_max_f32_e32 v55, 0, v31
	ds_read_b128 v[24:27], v39 offset:1216
	ds_read_b128 v[28:31], v39 offset:1472
	v_cvt_pk_f16_f32 v84, v52, v53
	s_waitcnt lgkmcnt(2)
	v_fma_f32 v20, v36, v20, v48
	v_fma_f32 v21, v36, v21, v49
	v_fma_f32 v22, v36, v22, v50
	v_fmac_f32_e32 v51, v36, v23
	v_max_f32_e32 v20, 0, v20
	v_max_f32_e32 v21, 0, v21
	v_max_f32_e32 v22, 0, v22
	v_max_f32_e32 v23, 0, v51
	v_cvt_pk_f16_f32 v87, v22, v23
	v_cvt_pk_f16_f32 v86, v20, v21
	ds_read_b128 v[20:23], v94
	ds_read_b128 v[48:51], v94 offset:1024
	s_waitcnt lgkmcnt(1)
	v_mfma_f32_32x32x16_f16 v[0:15], v[20:23], v[40:43], v[0:15]
	v_fma_f32 v24, v36, v24, v28
	v_max_f32_e32 v52, 0, v24
	v_fma_f32 v24, v36, v25, v29
	v_max_f32_e32 v53, 0, v24
	v_fma_f32 v24, v36, v26, v30
	v_cvt_pk_f16_f32 v85, v54, v55
	v_max_f32_e32 v54, 0, v24
	v_lshlrev_b32_e32 v24, 5, v37
	s_mov_b32 s0, 0x13400
	v_fmac_f32_e32 v31, v36, v27
	v_add3_u32 v28, v24, v38, s0
	ds_read_b128 v[24:27], v94 offset:2048
	s_waitcnt lgkmcnt(1)
	v_mfma_f32_32x32x16_f16 v[0:15], v[48:51], v[44:47], v[0:15]
	v_max_f32_e32 v55, 0, v31
	ds_read_b128 v[20:23], v39 offset:1488
	s_barrier
	ds_read_b128 v[88:91], v28
	ds_read_b128 v[28:31], v94 offset:3072
	v_cvt_pk_f16_f32 v37, v54, v55
	v_cmp_gt_u32_e32 vcc, 32, v92
	s_waitcnt lgkmcnt(2)
	v_fma_f32 v20, v36, v32, v20
	v_mfma_f32_32x32x16_f16 v[0:15], v[24:27], v[84:87], v[0:15]
	v_fma_f32 v21, v36, v33, v21
	v_fma_f32 v22, v36, v34, v22
	v_fmac_f32_e32 v23, v36, v35
	v_max_f32_e32 v20, 0, v20
	v_max_f32_e32 v21, 0, v21
	v_max_f32_e32 v22, 0, v22
	v_max_f32_e32 v23, 0, v23
	v_cvt_pk_f16_f32 v39, v22, v23
	v_cvt_pk_f16_f32 v38, v20, v21
	v_cvt_pk_f16_f32 v36, v52, v53
	ds_read_b128 v[20:23], v94 offset:4096
	ds_read_b128 v[32:35], v94 offset:5120
	s_waitcnt lgkmcnt(2)
	v_mfma_f32_32x32x16_f16 v[0:15], v[28:31], v[36:39], v[0:15]
	s_waitcnt lgkmcnt(1)
	v_mfma_f32_32x32x16_f16 v[0:15], v[20:23], v[88:91], v[0:15]
	ds_read_b128 v[20:23], v93 offset:160
	ds_read_b128 v[24:27], v93 offset:192
	ds_read_b128 v[28:31], v93 offset:224
	ds_read_b128 v[64:67], v93 offset:256
	s_waitcnt lgkmcnt(1)
	v_mfma_f32_32x32x16_f16 v[16:31], v[32:35], v[40:43], v[16:31]
	ds_read_b128 v[32:35], v94 offset:6144
	ds_read_b128 v[48:51], v94 offset:7168
	s_nop 3
	v_max_f32_e32 v4, v4, v4
	v_max_f32_e32 v5, v5, v5
	v_max_f32_e32 v6, v6, v6
	v_max_f32_e32 v7, v7, v7
	v_max_f32_e32 v4, 0, v4
	v_max_f32_e32 v5, 0, v5
	s_waitcnt lgkmcnt(1)
	v_mfma_f32_32x32x16_f16 v[16:31], v[32:35], v[44:47], v[16:31]
	v_max_f32_e32 v6, 0, v6
	v_max_f32_e32 v7, 0, v7
	v_max_f32_e32 v2, v2, v2
	v_max_f32_e32 v3, v3, v3
	v_max_f32_e32 v2, 0, v2
	v_max_f32_e32 v3, 0, v3
	v_max_f32_e32 v0, v0, v0
	s_waitcnt lgkmcnt(0)
	v_mfma_f32_32x32x16_f16 v[16:31], v[48:51], v[84:87], v[16:31]
	ds_read_b128 v[32:35], v94 offset:8192
	ds_read_b128 v[48:51], v94 offset:9216
	v_max_f32_e32 v1, v1, v1
	v_max_f32_e32 v0, 0, v0
	v_max_f32_e32 v1, 0, v1
	s_waitcnt lgkmcnt(1)
	v_mfma_f32_32x32x16_f16 v[16:31], v[32:35], v[36:39], v[16:31]
	ds_read_b128 v[32:35], v94 offset:10240
	s_waitcnt lgkmcnt(1)
	v_mfma_f32_32x32x16_f16 v[16:31], v[48:51], v[88:91], v[16:31]
	ds_read_b128 v[68:71], v93 offset:288
	ds_read_b128 v[72:75], v93 offset:320
	ds_read_b128 v[76:79], v93 offset:352
	ds_read_b128 v[48:51], v93 offset:384
	ds_read_b128 v[52:55], v94 offset:11264
	s_waitcnt lgkmcnt(2)
	v_mfma_f32_32x32x16_f16 v[64:79], v[32:35], v[40:43], v[64:79]
	s_waitcnt lgkmcnt(0)
	v_mfma_f32_32x32x16_f16 v[64:79], v[52:55], v[44:47], v[64:79]
	ds_read_b128 v[32:35], v94 offset:12288
	ds_read_b128 v[52:55], v94 offset:13312
	s_waitcnt lgkmcnt(1)
	v_mfma_f32_32x32x16_f16 v[64:79], v[32:35], v[84:87], v[64:79]
	ds_read_b128 v[32:35], v94 offset:14336
	ds_read_b128 v[96:99], v94 offset:15360
	s_waitcnt lgkmcnt(2)
	v_mfma_f32_32x32x16_f16 v[64:79], v[52:55], v[36:39], v[64:79]
	s_waitcnt lgkmcnt(1)
	v_mfma_f32_32x32x16_f16 v[64:79], v[32:35], v[88:91], v[64:79]
	ds_read_b128 v[52:55], v93 offset:416
	ds_read_b128 v[56:59], v93 offset:448
	ds_read_b128 v[60:63], v93 offset:480
	ds_read_b128 v[32:35], v93 offset:512
	s_waitcnt lgkmcnt(1)
	v_mfma_f32_32x32x16_f16 v[48:63], v[96:99], v[40:43], v[48:63]
	ds_read_b128 v[40:43], v94 offset:16384
	ds_read_b128 v[96:99], v94 offset:17408
	s_waitcnt lgkmcnt(1)
	v_mfma_f32_32x32x16_f16 v[48:63], v[40:43], v[44:47], v[48:63]
	ds_read_b128 v[40:43], v94 offset:18432
	ds_read_b128 v[44:47], v94 offset:19456
	s_waitcnt lgkmcnt(2)
	v_mfma_f32_32x32x16_f16 v[48:63], v[96:99], v[84:87], v[48:63]
	v_cvt_pk_f16_f32 v87, v6, v7
	v_cvt_pk_f16_f32 v86, v4, v5
	v_max_f32_e32 v4, v12, v12
	v_max_f32_e32 v5, v13, v13
	v_max_f32_e32 v6, v14, v14
	v_max_f32_e32 v7, v15, v15
	v_max_f32_e32 v4, 0, v4
	s_waitcnt lgkmcnt(1)
	v_mfma_f32_32x32x16_f16 v[48:63], v[40:43], v[36:39], v[48:63]
	v_max_f32_e32 v5, 0, v5
	v_max_f32_e32 v6, 0, v6
	v_max_f32_e32 v7, 0, v7
	v_cvt_pk_f16_f32 v85, v2, v3
	v_max_f32_e32 v2, v10, v10
	v_max_f32_e32 v3, v11, v11
	v_max_f32_e32 v2, 0, v2
	s_waitcnt lgkmcnt(0)
	v_mfma_f32_32x32x16_f16 v[48:63], v[44:47], v[88:91], v[48:63]
	v_cvt_pk_f16_f32 v91, v6, v7
	v_cvt_pk_f16_f32 v90, v4, v5
	v_max_f32_e32 v4, v20, v20
	v_max_f32_e32 v5, v21, v21
	v_max_f32_e32 v6, v22, v22
	v_max_f32_e32 v7, v23, v23
	v_max_f32_e32 v3, 0, v3
	v_max_f32_e32 v4, 0, v4
	v_max_f32_e32 v5, 0, v5
	v_max_f32_e32 v6, 0, v6
	v_max_f32_e32 v7, 0, v7
	v_cvt_pk_f16_f32 v89, v2, v3
	v_max_f32_e32 v2, v18, v18
	v_max_f32_e32 v3, v19, v19
	v_cvt_pk_f16_f32 v19, v6, v7
	v_cvt_pk_f16_f32 v18, v4, v5
	v_max_f32_e32 v4, v28, v28
	v_max_f32_e32 v5, v29, v29
	v_max_f32_e32 v6, v30, v30
	v_max_f32_e32 v7, v31, v31
	v_max_f32_e32 v4, 0, v4
	v_max_f32_e32 v5, 0, v5
	v_max_f32_e32 v6, 0, v6
	v_max_f32_e32 v7, 0, v7
	v_cvt_pk_f16_f32 v84, v0, v1
	v_max_f32_e32 v0, v8, v8
	v_max_f32_e32 v1, v9, v9
	v_cvt_pk_f16_f32 v23, v6, v7
	v_cvt_pk_f16_f32 v22, v4, v5
	v_max_f32_e32 v4, v68, v68
	v_max_f32_e32 v5, v69, v69
	v_max_f32_e32 v6, v70, v70
	v_max_f32_e32 v7, v71, v71
	v_max_f32_e32 v0, 0, v0
	v_max_f32_e32 v1, 0, v1
	v_max_f32_e32 v2, 0, v2
	v_max_f32_e32 v3, 0, v3
	v_max_f32_e32 v4, 0, v4
	v_max_f32_e32 v5, 0, v5
	v_max_f32_e32 v6, 0, v6
	v_max_f32_e32 v7, 0, v7
	v_cvt_pk_f16_f32 v88, v0, v1
	v_max_f32_e32 v0, v16, v16
	v_max_f32_e32 v1, v17, v17
	v_cvt_pk_f16_f32 v17, v2, v3
	v_max_f32_e32 v2, v26, v26
	v_max_f32_e32 v3, v27, v27
	v_cvt_pk_f16_f32 v27, v6, v7
	v_cvt_pk_f16_f32 v26, v4, v5
	ds_read_b128 v[4:7], v94 offset:20480
	v_max_f32_e32 v0, 0, v0
	v_max_f32_e32 v1, 0, v1
	v_cvt_pk_f16_f32 v16, v0, v1
	v_max_f32_e32 v0, v24, v24
	v_max_f32_e32 v1, v25, v25
	v_max_f32_e32 v0, 0, v0
	v_max_f32_e32 v1, 0, v1
	v_cvt_pk_f16_f32 v20, v0, v1
	v_max_f32_e32 v0, v64, v64
	v_max_f32_e32 v1, v65, v65
	ds_read_b128 v[36:39], v93 offset:544
	ds_read_b128 v[40:43], v93 offset:576
	ds_read_b128 v[44:47], v93 offset:608
	v_max_f32_e32 v0, 0, v0
	v_max_f32_e32 v1, 0, v1
	v_cvt_pk_f16_f32 v24, v0, v1
	v_max_f32_e32 v0, v72, v72
	v_max_f32_e32 v2, 0, v2
	v_max_f32_e32 v3, 0, v3
	v_max_f32_e32 v12, 0, v0
	v_max_f32_e32 v0, v73, v73
	v_cvt_pk_f16_f32 v21, v2, v3
	v_max_f32_e32 v2, v66, v66
	v_max_f32_e32 v3, v67, v67
	v_max_f32_e32 v13, 0, v0
	v_max_f32_e32 v0, v74, v74
	v_max_f32_e32 v2, 0, v2
	v_max_f32_e32 v3, 0, v3
	v_max_f32_e32 v14, 0, v0
	v_max_f32_e32 v0, v75, v75
	s_waitcnt lgkmcnt(0)
	v_mfma_f32_32x32x16_f16 v[32:47], v[4:7], v[84:87], v[32:47]
	v_cvt_pk_f16_f32 v25, v2, v3
	v_max_f32_e32 v15, 0, v0
	v_max_f32_e32 v0, v76, v76
	v_max_f32_e32 v1, v77, v77
	v_max_f32_e32 v2, v78, v78
	v_max_f32_e32 v3, v79, v79
	v_max_f32_e32 v0, 0, v0
	v_max_f32_e32 v1, 0, v1
	v_max_f32_e32 v2, 0, v2
	v_max_f32_e32 v3, 0, v3
	v_cvt_pk_f16_f32 v31, v2, v3
	v_cvt_pk_f16_f32 v30, v0, v1
	ds_read_b128 v[0:3], v93 offset:640
	ds_read_b128 v[8:11], v94 offset:21504
	v_max_f32_e32 v4, v48, v48
	v_cvt_pk_f16_f32 v28, v12, v13
	v_max_f32_e32 v12, 0, v4
	v_max_f32_e32 v4, v49, v49
	v_max_f32_e32 v13, 0, v4
	ds_read_b128 v[4:7], v94 offset:22528
	s_waitcnt lgkmcnt(1)
	v_mfma_f32_32x32x16_f16 v[32:47], v[8:11], v[88:91], v[32:47]
	v_max_f32_e32 v8, v50, v50
	v_cvt_pk_f16_f32 v29, v14, v15
	v_max_f32_e32 v14, 0, v8
	v_max_f32_e32 v8, v51, v51
	v_max_f32_e32 v15, 0, v8
	v_max_f32_e32 v8, v52, v52
	v_max_f32_e32 v48, 0, v8
	ds_read_b128 v[8:11], v94 offset:23552
	s_waitcnt lgkmcnt(1)
	v_mfma_f32_32x32x16_f16 v[32:47], v[4:7], v[16:19], v[32:47]
	v_max_f32_e32 v4, v53, v53
	v_max_f32_e32 v49, 0, v4
	v_max_f32_e32 v4, v54, v54
	v_max_f32_e32 v50, 0, v4
	v_max_f32_e32 v4, v55, v55
	v_max_f32_e32 v51, 0, v4
	ds_read_b128 v[4:7], v94 offset:24576
	s_waitcnt lgkmcnt(1)
	v_mfma_f32_32x32x16_f16 v[32:47], v[8:11], v[20:23], v[32:47]
	v_max_f32_e32 v8, v56, v56
	v_cvt_pk_f16_f32 v51, v50, v51
	v_cvt_pk_f16_f32 v50, v48, v49
	v_cvt_pk_f16_f32 v48, v12, v13
	v_max_f32_e32 v12, 0, v8
	ds_read_b128 v[8:11], v94 offset:25600
	v_cvt_pk_f16_f32 v49, v14, v15
	s_waitcnt lgkmcnt(1)
	v_mfma_f32_32x32x16_f16 v[32:47], v[4:7], v[24:27], v[32:47]
	v_max_f32_e32 v4, v57, v57
	v_max_f32_e32 v13, 0, v4
	v_max_f32_e32 v4, v58, v58
	v_max_f32_e32 v14, 0, v4
	v_max_f32_e32 v4, v59, v59
	v_max_f32_e32 v15, 0, v4
	ds_read_b128 v[4:7], v94 offset:26624
	s_waitcnt lgkmcnt(1)
	v_mfma_f32_32x32x16_f16 v[32:47], v[8:11], v[28:31], v[32:47]
	v_max_f32_e32 v8, v60, v60
	v_max_f32_e32 v52, 0, v8
	v_max_f32_e32 v8, v61, v61
	v_max_f32_e32 v53, 0, v8
	v_max_f32_e32 v8, v62, v62
	v_max_f32_e32 v54, 0, v8
	ds_read_b128 v[8:11], v94 offset:27648
	s_waitcnt lgkmcnt(1)
	v_mfma_f32_32x32x16_f16 v[32:47], v[4:7], v[48:51], v[32:47]
	ds_read_b128 v[56:59], v94 offset:28672
	v_max_f32_e32 v4, v63, v63
	v_max_f32_e32 v4, 0, v4
	v_cvt_pk_f16_f32 v55, v54, v4
	v_cvt_pk_f16_f32 v54, v52, v53
	v_cvt_pk_f16_f32 v53, v14, v15
	v_cvt_pk_f16_f32 v52, v12, v13
	s_waitcnt lgkmcnt(1)
	s_nop 0
	v_mfma_f32_32x32x16_f16 v[32:47], v[8:11], v[52:55], v[32:47]
	ds_read_b128 v[4:7], v93 offset:672
	ds_read_b128 v[8:11], v93 offset:704
	ds_read_b128 v[12:15], v93 offset:736
	ds_read_b128 v[60:63], v94 offset:29696
	ds_read_b128 v[64:67], v93 offset:768
	s_waitcnt lgkmcnt(2)
	v_mfma_f32_32x32x16_f16 v[0:15], v[56:59], v[84:87], v[0:15]
	s_waitcnt lgkmcnt(1)
	v_mfma_f32_32x32x16_f16 v[0:15], v[60:63], v[88:91], v[0:15]
	ds_read_b128 v[56:59], v94 offset:30720
	ds_read_b128 v[60:63], v94 offset:31744
	s_waitcnt lgkmcnt(1)
	v_mfma_f32_32x32x16_f16 v[0:15], v[56:59], v[16:19], v[0:15]
	s_waitcnt lgkmcnt(0)
	v_mfma_f32_32x32x16_f16 v[0:15], v[60:63], v[20:23], v[0:15]
	ds_read_b128 v[16:19], v94 offset:32768
	ds_read_b128 v[20:23], v94 offset:33792
	s_waitcnt lgkmcnt(1)
	v_mfma_f32_32x32x16_f16 v[0:15], v[16:19], v[24:27], v[0:15]
	s_waitcnt lgkmcnt(0)
	v_mfma_f32_32x32x16_f16 v[0:15], v[20:23], v[28:31], v[0:15]
	ds_read_b128 v[16:19], v94 offset:34816
	ds_read_b128 v[20:23], v94 offset:35840
	s_waitcnt lgkmcnt(1)
	v_mfma_f32_32x32x16_f16 v[0:15], v[16:19], v[48:51], v[0:15]
	v_max_f32_e32 v16, v32, v32
	v_max_f32_e32 v16, 0, v16
	v_max_f32_e32 v17, v33, v33
	v_fma_f32 v16, v64, v16, 0
	v_max_f32_e32 v17, 0, v17
	v_fmac_f32_e32 v16, v65, v17
	v_max_f32_e32 v17, v34, v34
	s_waitcnt lgkmcnt(0)
	v_mfma_f32_32x32x16_f16 v[0:15], v[20:23], v[52:55], v[0:15]
	v_max_f32_e32 v17, 0, v17
	ds_read_b128 v[18:21], v93 offset:800
	ds_read_b128 v[22:25], v93 offset:832
	v_fmac_f32_e32 v16, v66, v17
	v_max_f32_e32 v17, v35, v35
	v_max_f32_e32 v17, 0, v17
	v_fmac_f32_e32 v16, v67, v17
	v_max_f32_e32 v17, v36, v36
	v_max_f32_e32 v17, 0, v17
	s_waitcnt lgkmcnt(1)
	v_fmac_f32_e32 v16, v18, v17
	v_max_f32_e32 v17, v37, v37
	v_max_f32_e32 v17, 0, v17
	v_fmac_f32_e32 v16, v19, v17
	v_max_f32_e32 v17, v38, v38
	v_max_f32_e32 v17, 0, v17
	v_fmac_f32_e32 v16, v20, v17
	v_max_f32_e32 v17, v39, v39
	v_max_f32_e32 v17, 0, v17
	v_fmac_f32_e32 v16, v21, v17
	v_max_f32_e32 v17, v40, v40
	v_max_f32_e32 v17, 0, v17
	s_waitcnt lgkmcnt(0)
	v_fmac_f32_e32 v16, v22, v17
	v_max_f32_e32 v17, v41, v41
	v_max_f32_e32 v17, 0, v17
	v_fmac_f32_e32 v16, v23, v17
	v_max_f32_e32 v17, v42, v42
	v_max_f32_e32 v17, 0, v17
	ds_read_b128 v[18:21], v93 offset:864
	v_fmac_f32_e32 v16, v24, v17
	v_max_f32_e32 v17, v43, v43
	v_max_f32_e32 v17, 0, v17
	v_fmac_f32_e32 v16, v25, v17
	v_max_f32_e32 v17, v44, v44
	v_max_f32_e32 v17, 0, v17
	ds_read_b128 v[22:25], v93 offset:896
	s_waitcnt lgkmcnt(1)
	v_fmac_f32_e32 v16, v18, v17
	v_max_f32_e32 v17, v45, v45
	v_max_f32_e32 v17, 0, v17
	v_fmac_f32_e32 v16, v19, v17
	v_max_f32_e32 v17, v46, v46
	v_max_f32_e32 v17, 0, v17
	v_fmac_f32_e32 v16, v20, v17
	v_max_f32_e32 v17, v47, v47
	v_max_f32_e32 v17, 0, v17
	v_max_f32_e32 v0, v0, v0
	v_fmac_f32_e32 v16, v21, v17
	v_max_f32_e32 v0, 0, v0
	s_waitcnt lgkmcnt(0)
	v_fmac_f32_e32 v16, v22, v0
	v_max_f32_e32 v0, v1, v1
	v_max_f32_e32 v0, 0, v0
	v_fmac_f32_e32 v16, v23, v0
	v_max_f32_e32 v0, v2, v2
	v_max_f32_e32 v0, 0, v0
	v_fmac_f32_e32 v16, v24, v0
	v_max_f32_e32 v0, v3, v3
	v_max_f32_e32 v17, 0, v0
	ds_read_b128 v[0:3], v93 offset:928
	ds_read_b128 v[18:21], v93 offset:960
	v_max_f32_e32 v4, v4, v4
	v_fmac_f32_e32 v16, v25, v17
	v_max_f32_e32 v4, 0, v4
	s_waitcnt lgkmcnt(1)
	v_fmac_f32_e32 v16, v0, v4
	v_max_f32_e32 v0, v5, v5
	v_max_f32_e32 v0, 0, v0
	v_fmac_f32_e32 v16, v1, v0
	v_max_f32_e32 v0, v6, v6
	v_max_f32_e32 v0, 0, v0
	v_fmac_f32_e32 v16, v2, v0
	v_max_f32_e32 v0, v7, v7
	v_max_f32_e32 v0, 0, v0
	v_fmac_f32_e32 v16, v3, v0
	v_max_f32_e32 v0, v8, v8
	v_max_f32_e32 v0, 0, v0
	s_waitcnt lgkmcnt(0)
	v_fmac_f32_e32 v16, v18, v0
	v_max_f32_e32 v0, v9, v9
	v_max_f32_e32 v0, 0, v0
	v_fmac_f32_e32 v16, v19, v0
	v_max_f32_e32 v0, v10, v10
	v_max_f32_e32 v0, 0, v0
	v_fmac_f32_e32 v16, v20, v0
	v_max_f32_e32 v0, v11, v11
	v_max_f32_e32 v0, 0, v0
	v_fmac_f32_e32 v16, v21, v0
	v_max_f32_e32 v0, v12, v12
	v_max_f32_e32 v0, 0, v0
	v_fmac_f32_e32 v16, v80, v0
	v_max_f32_e32 v0, v13, v13
	v_max_f32_e32 v0, 0, v0
	v_fmac_f32_e32 v16, v81, v0
	v_max_f32_e32 v0, v14, v14
	v_max_f32_e32 v0, 0, v0
	v_fmac_f32_e32 v16, v82, v0
	v_max_f32_e32 v0, v15, v15
	v_max_f32_e32 v0, 0, v0
	v_fmac_f32_e32 v16, v83, v0
	v_mov_b32_e32 v0, v16
	s_nop 1
	v_permlane32_swap_b32_e32 v16, v0
	s_and_saveexec_b64 s[0:1], vcc
	s_cbranch_execz .LBB0_123
	s_mov_b32 s0, s88
	v_add_f32_e32 v0, v16, v0
	s_waitcnt lgkmcnt(0)
	v_add_f32_e32 v0, s0, v0
	v_mul_f32_e32 v0, 0xbfb8aa3b, v0
	v_exp_f32_e32 v1, v0
	s_or_b32 s0, s31, s30
	v_or_b32_e32 v0, s0, v92
	v_add_f32_e32 v2, 1.0, v1
	v_div_scale_f32 v3, s[0:1], v2, v2, 1.0
	v_rcp_f32_e32 v4, v3
	v_div_scale_f32 v5, vcc, 1.0, v2, 1.0
	v_ashrrev_i32_e32 v1, 31, v0
	v_fma_f32 v6, -v3, v4, 1.0
	v_fmac_f32_e32 v4, v6, v4
	v_mul_f32_e32 v6, v5, v4
	v_fma_f32 v7, -v3, v6, v5
	v_fmac_f32_e32 v6, v7, v4
	v_fma_f32 v3, -v3, v6, v5
	v_div_fmas_f32 v3, v3, v4, v6
	v_div_fixup_f32 v2, v3, v2, 1.0
	v_lshl_add_u64 v[0:1], v[0:1], 2, s[22:23]
	global_store_dword v[0:1], v2, off

.Lmlp_others:
	s_barrier
	s_endpgm
